# combined: all fp8 weight conversion in the hand-written tile loop, P-fragment lane swaps removed via V read addressing, 4-bit K swizzle for GQA
# speedup vs baseline: 1.0101x; 1.0064x over previous
.LBB0_912:
	s_load_dwordx2 s[26:27], s[2:3], 0x78
	s_ashr_i32 s2, s54, 4
	s_mul_hi_i32 s3, s2, 0x2aaaaaab
	s_lshr_b32 s4, s3, 31
	s_add_i32 s3, s3, s4
	s_mul_i32 s3, s3, 6
	s_sub_i32 s2, s2, s3
	s_mul_hi_i32 s3, s54, 0x2aaaaaab
	s_lshr_b32 s4, s3, 31
	s_ashr_i32 s3, s3, 4
	s_add_i32 s28, s3, s4
	s_mul_i32 s3, s2, 0x56
	s_lshr_b32 s4, s3, 8
	s_bfe_u32 s3, s3, 0x1000f
	s_add_i32 s4, s4, s3
	s_ashr_i32 s29, s28, 31
	s_lshl_b32 s3, s54, 8
	s_lshl_b64 s[30:31], s[28:29], 12
	s_and_b32 s3, s3, 0xf00
	s_or_b32 s30, s30, s3
	s_sext_i32_i8 s34, s4
	s_mul_i32 s3, s31, 0x600
	s_mul_hi_u32 s4, s30, 0x600
	s_add_i32 s4, s4, s3
	s_mul_i32 s3, s30, 0x600
	s_add_u32 s5, s24, s3
	s_addc_u32 s4, s25, s4
	s_lshl_b32 s22, s2, 7
	s_ashr_i32 s23, s22, 31
	s_lshl_b64 s[2:3], s[22:23], 1
	s_add_u32 s2, s5, s2
	s_addc_u32 s3, s4, s3
	s_add_u32 s38, s2, 0x48560200
	s_addc_u32 s39, s3, 0
	s_lshl_b64 s[4:5], s[28:29], 21
	s_add_u32 s37, s24, s4
	s_addc_u32 s40, s25, s5
	s_lshl_b32 s2, s34, 7
	s_ashr_i32 s3, s2, 31
	s_lshl_b64 s[34:35], s[2:3], 1
	s_add_u32 s2, s37, s34
	s_addc_u32 s3, s40, s35
	s_add_u32 s2, s2, 0x49d60200
	s_addc_u32 s3, s3, 0
	s_lshl_b64 s[28:29], s[28:29], 25
	s_add_u32 s37, s24, s28
	s_addc_u32 s40, s25, s29
	s_add_u32 s37, s37, s34
	s_waitcnt lgkmcnt(0)
	s_addc_u32 s40, s40, s35
	s_add_u32 s52, s37, 0x40560a00
	v_ashrrev_i32_e32 v54, 4, v0
	v_lshlrev_b32_e32 v1, 3, v0
	v_ashrrev_i32_e32 v55, 31, v54
	s_addc_u32 s53, s40, 0
	v_and_b32_e32 v2, 0x78, v1
	v_lshlrev_b64 v[48:49], 13, v[54:55]
	v_lshlrev_b32_e32 v52, 1, v2
	v_add_u32_e32 v18, 32, v54
	v_lshl_add_u64 v[2:3], s[52:53], 0, v[48:49]
	v_mov_b32_e32 v53, v177
	v_lshl_add_u64 v[2:3], v[2:3], 0, v[52:53]
	v_ashrrev_i32_e32 v19, 31, v18
	global_load_dwordx4 v[2:5], v[2:3], off
	v_lshlrev_b64 v[6:7], 13, v[18:19]
	v_lshlrev_b64 v[50:51], 9, v[54:55]
	v_lshl_add_u64 v[6:7], s[52:53], 0, v[6:7]
	v_lshl_add_u64 v[10:11], s[2:3], 0, v[50:51]
	v_lshl_add_u64 v[6:7], v[6:7], 0, v[52:53]
	v_lshl_add_u64 v[10:11], v[10:11], 0, v[52:53]
	global_load_dwordx4 v[6:9], v[6:7], off
	v_lshlrev_b64 v[14:15], 9, v[18:19]
	global_load_dwordx4 v[10:13], v[10:11], off
	v_lshl_add_u64 v[14:15], s[2:3], 0, v[14:15]
	v_lshl_add_u64 v[14:15], v[14:15], 0, v[52:53]
	v_readfirstlane_b32 s37, v0
	global_load_dwordx4 v[14:17], v[14:15], off
	s_ashr_i32 s40, s37, 1
	v_mov_b32_e32 v19, s40
	v_bfe_u32 v22, v0, 5, 1
	v_bfi_b32 v19, s1, v19, v0
	v_mov_b64_e32 v[20:21], s[38:39]
	v_mad_i64_i32 v[20:21], s[38:39], v19, s0, v[20:21]
	v_lshlrev_b32_e32 v176, 4, v22
	v_lshl_add_u64 v[20:21], v[20:21], 0, v[176:177]
	global_load_dwordx4 v[124:127], v[20:21], off
	global_load_dwordx4 v[120:123], v[20:21], off offset:32
	global_load_dwordx4 v[116:119], v[20:21], off offset:64
	global_load_dwordx4 v[112:115], v[20:21], off offset:96
	global_load_dwordx4 v[108:111], v[20:21], off offset:128
	global_load_dwordx4 v[104:107], v[20:21], off offset:160
	global_load_dwordx4 v[100:103], v[20:21], off offset:192
	global_load_dwordx4 v[96:99], v[20:21], off offset:224
	v_and_b32_e32 v19, 0xfffff0, v54
	v_lshlrev_b32_e32 v20, 1, v54
	v_mov_b32_e32 v216, v22
	v_and_or_b32 v19, v20, 8, v19
	v_and_b32_e32 v22, 0xfffff0, v18
	v_lshlrev_b32_e32 v23, 1, v18
	v_lshrrev_b32_e32 v20, 1, v54
	v_lshrrev_b32_e32 v19, 1, v19
	v_bfe_u32 v1, v1, 5, 2
	v_and_b32_e32 v21, 3, v54
	v_and_or_b32 v22, v23, 8, v22
	v_or_b32_e32 v19, v19, v1
	v_and_or_b32 v20, v20, 4, v21
	v_lshrrev_b32_e32 v22, 1, v22
	v_lshlrev_b32_e32 v19, 9, v19
	v_lshlrev_b32_e32 v20, 6, v20
	v_and_b32_e32 v21, 48, v52
	v_or_b32_e32 v1, v22, v1
	v_or3_b32 v19, v19, v20, v21
	v_lshlrev_b32_e32 v1, 9, v1
	v_or3_b32 v1, v1, v20, v21
	v_add_u32_e32 v193, 0, v19
	s_waitcnt vmcnt(0)
	v_add_u32_e32 v194, 0, v1
	v_lshlrev_b32_e32 v1, 8, v54
	v_and_b32_e32 v178, 31, v0
	v_lshlrev_b32_e32 v78, 4, v0
	v_and_b32_e32 v79, 63, v0
	v_add_u32_e32 v64, 64, v54
	v_add_u32_e32 v66, 0x60, v54
	v_ashrrev_i32_e32 v65, 31, v64
	v_ashrrev_i32_e32 v67, 31, v66
	v_add_u32_e32 v72, 0xa0, v54
	v_ashrrev_i32_e32 v73, 31, v72
	v_add_u32_e32 v54, 0x80, v54
	v_lshlrev_b64 v[74:75], 9, v[72:73]
	v_lshlrev_b64 v[72:73], 13, v[72:73]
	v_lshl_add_u64 v[74:75], s[2:3], 0, v[74:75]
	v_lshl_add_u64 v[72:73], s[52:53], 0, v[72:73]
	v_lshl_add_u64 v[74:75], v[74:75], 0, v[52:53]
	v_lshl_add_u64 v[72:73], v[72:73], 0, v[52:53]
	s_and_b32 s37, s37, 0x3fffffc0
	s_lshl_b32 s37, s37, 2
	s_add_i32 s56, s37, 0
	s_add_i32 s56, s56, 0x10000
	s_and_b32 s55, s40, 0xffffffe0
	s_cmp_lg_u32 0, -1
	s_cselect_b32 s58, 0, 0
	s_mov_b32 s37, s36
	s_mov_b32 s38, s36
	s_mov_b32 s39, s36
	s_mov_b32 s40, s36
	s_mov_b32 s41, s36
	s_mov_b32 s42, s36
	s_mov_b32 s43, s36
	s_waitcnt vmcnt(11)
	ds_write_b128 v193, v[2:5]
	v_and_b32_e32 v2, 0xf0, v0
	v_bitop3_b32 v1, v52, v1, v2 bitop3:0xde
	v_add_u32_e32 v195, 0, v1
	v_lshlrev_b32_e32 v1, 8, v18
	v_bitop3_b32 v1, v52, v1, v2 bitop3:0xde
	v_add_u32_e32 v196, 0, v1
	s_waitcnt vmcnt(10)
	ds_write_b128 v194, v[6:9]
	s_mov_b32 s44, s36
	s_waitcnt vmcnt(9)
	ds_write_b128 v195, v[10:13] offset:32768
	v_lshlrev_b32_e32 v10, 8, v178
	v_and_b32_e32 v11, 0xf0, v78
	v_bitop3_b32 v1, v176, v10, v11 bitop3:0xde
	v_add_u32_e32 v197, 0, v1
	s_waitcnt vmcnt(8)
	ds_write_b128 v196, v[14:17] offset:32768
	s_waitcnt lgkmcnt(0)
	s_barrier
	ds_read_b128 v[2:5], v197 offset:32768
	ds_read_b128 v[6:9], v197 offset:40960
	s_waitcnt vmcnt(7) lgkmcnt(1)
	v_mfma_f32_32x32x16_bf16 v[32:47], v[2:5], v[124:127], 0
	v_or_b32_e32 v1, 32, v176
	v_bitop3_b32 v1, v1, v10, v11 bitop3:0xde
	v_add_u32_e32 v198, 0, v1
	v_or_b32_e32 v1, 64, v176
	v_bitop3_b32 v1, v1, v10, v11 bitop3:0xde
	v_add_u32_e32 v199, 0, v1
	v_or_b32_e32 v1, 0x60, v176
	s_waitcnt lgkmcnt(0)
	v_mfma_f32_32x32x16_bf16 v[16:31], v[6:9], v[124:127], 0
	ds_read_b128 v[2:5], v198 offset:32768
	ds_read_b128 v[6:9], v198 offset:40960
	v_bitop3_b32 v1, v1, v10, v11 bitop3:0xde
	v_add_u32_e32 v200, 0, v1
	v_or_b32_e32 v1, 0x80, v176
	v_bitop3_b32 v1, v1, v10, v11 bitop3:0xde
	v_add_u32_e32 v201, 0, v1
	v_or_b32_e32 v1, 0xa0, v176
	s_waitcnt vmcnt(6) lgkmcnt(1)
	v_mfma_f32_32x32x16_bf16 v[32:47], v[2:5], v[120:123], v[32:47]
	v_bitop3_b32 v1, v1, v10, v11 bitop3:0xde
	v_add_u32_e32 v202, 0, v1
	v_lshlrev_b32_e32 v12, 3, v79
	v_and_b32_e32 v1, 0xc0, v78
	s_mov_b32 s45, s36
	s_mov_b32 s46, s36
	s_mov_b32 s47, s36
	s_waitcnt lgkmcnt(0)
	v_mfma_f32_32x32x16_bf16 v[16:31], v[6:9], v[120:123], v[16:31]
	ds_read_b128 v[2:5], v199 offset:32768
	ds_read_b128 v[6:9], v199 offset:40960
	s_mov_b32 s48, s36
	s_mov_b32 s49, s36
	s_mov_b32 s50, s36
	s_mov_b32 s51, s36
	s_mov_b32 s57, 1
	v_lshl_add_u32 v179, v178, 2, s56
	s_waitcnt vmcnt(5) lgkmcnt(1)
	v_mfma_f32_32x32x16_bf16 v[32:47], v[2:5], v[116:119], v[32:47]
	v_mov_b32_e32 v190, 0
	s_waitcnt lgkmcnt(0)
	v_mfma_f32_32x32x16_bf16 v[16:31], v[6:9], v[116:119], v[16:31]
	ds_read_b128 v[2:5], v200 offset:32768
	ds_read_b128 v[6:9], v200 offset:40960
	s_waitcnt vmcnt(4) lgkmcnt(1)
	v_mfma_f32_32x32x16_bf16 v[32:47], v[2:5], v[112:115], v[32:47]
	s_waitcnt lgkmcnt(0)
	v_mfma_f32_32x32x16_bf16 v[16:31], v[6:9], v[112:115], v[16:31]
	ds_read_b128 v[2:5], v201 offset:32768
	ds_read_b128 v[6:9], v201 offset:40960
	s_waitcnt vmcnt(3) lgkmcnt(1)
	v_mfma_f32_32x32x16_bf16 v[32:47], v[2:5], v[108:111], v[32:47]
	ds_read_b128 v[2:5], v202 offset:32768
	s_waitcnt lgkmcnt(1)
	v_mfma_f32_32x32x16_bf16 v[16:31], v[6:9], v[108:111], v[16:31]
	ds_read_b128 v[6:9], v202 offset:40960
	s_waitcnt vmcnt(2) lgkmcnt(1)
	v_mfma_f32_32x32x16_bf16 v[32:47], v[2:5], v[104:107], v[32:47]
	v_lshlrev_b32_e32 v5, 1, v0
	v_or_b32_e32 v0, 0xc0, v176
	v_bitop3_b32 v0, v0, v10, v11 bitop3:0xde
	v_add_u32_e32 v203, 0, v0
	v_and_or_b32 v4, v12, 24, v1
	ds_read_b128 v[0:3], v203 offset:32768
	v_and_b32_e32 v5, 32, v5
	s_waitcnt lgkmcnt(1)
	v_mfma_f32_32x32x16_bf16 v[16:31], v[6:9], v[104:107], v[16:31]
	v_lshlrev_b32_e32 v6, 3, v12
	v_and_b32_e32 v6, 0x800, v6
	v_or3_b32 v80, v4, v5, v6
	ds_read_b128 v[4:7], v203 offset:40960
	v_add_u32_e32 v192, s58, v80
	s_waitcnt vmcnt(1) lgkmcnt(1)
	v_mfma_f32_32x32x16_bf16 v[32:47], v[0:3], v[100:103], v[32:47]
	v_or_b32_e32 v0, 0xe0, v176
	v_bitop3_b32 v0, v0, v10, v11 bitop3:0xde
	v_add_u32_e32 v204, 0, v0
	ds_read_b128 v[0:3], v204 offset:32768
	ds_read_b128 v[56:59], v204 offset:40960
	s_waitcnt lgkmcnt(2)
	v_mfma_f32_32x32x16_bf16 v[16:31], v[4:7], v[100:103], v[16:31]
	s_waitcnt vmcnt(0) lgkmcnt(1)
	v_mfma_f32_32x32x16_bf16 v[32:47], v[0:3], v[96:99], v[32:47]
	v_mov_b64_e32 v[0:1], s[36:37]
	v_mov_b64_e32 v[14:15], s[50:51]
	v_mov_b64_e32 v[2:3], s[38:39]
	v_mov_b64_e32 v[4:5], s[40:41]
	v_mov_b64_e32 v[6:7], s[42:43]
	v_mov_b64_e32 v[8:9], s[44:45]
	v_mov_b64_e32 v[10:11], s[46:47]
	s_waitcnt lgkmcnt(0)
	v_mfma_f32_32x32x16_bf16 v[16:31], v[56:59], v[96:99], v[16:31]
	s_nop 2
	v_max_f32_e32 v55, v33, v33
	v_max_f32_e32 v56, v32, v32
	v_max_f32_e32 v55, v56, v55
	v_max3_f32 v55, v55, v34, v35
	v_max3_f32 v55, v55, v36, v37
	v_max3_f32 v55, v55, v38, v39
	v_max3_f32 v55, v55, v40, v41
	v_max3_f32 v55, v55, v42, v43
	v_max3_f32 v55, v55, v44, v45
	v_max3_f32 v55, v55, v46, v47
	v_max3_f32 v55, v55, v16, v17
	v_max3_f32 v55, v55, v18, v19
	v_max3_f32 v55, v55, v20, v21
	v_max3_f32 v55, v55, v22, v23
	v_max3_f32 v55, v55, v24, v25
	v_max3_f32 v55, v55, v26, v27
	v_lshlrev_b64 v[56:57], 13, v[64:65]
	v_lshlrev_b64 v[58:59], 13, v[66:67]
	v_lshlrev_b64 v[64:65], 9, v[64:65]
	v_lshlrev_b64 v[66:67], 9, v[66:67]
	v_max3_f32 v55, v55, v28, v29
	v_lshl_add_u64 v[56:57], s[52:53], 0, v[56:57]
	v_lshl_add_u64 v[58:59], s[52:53], 0, v[58:59]
	v_lshl_add_u64 v[64:65], s[2:3], 0, v[64:65]
	v_lshl_add_u64 v[66:67], s[2:3], 0, v[66:67]
	v_max3_f32 v81, v55, v30, v31
	v_lshl_add_u64 v[56:57], v[56:57], 0, v[52:53]
	v_lshl_add_u64 v[60:61], v[58:59], 0, v[52:53]
	v_lshl_add_u64 v[64:65], v[64:65], 0, v[52:53]
	v_lshl_add_u64 v[68:69], v[66:67], 0, v[52:53]
	v_ashrrev_i32_e32 v55, 31, v54
	global_load_dwordx4 v[56:59], v[56:57], off
	s_nop 0
	global_load_dwordx4 v[60:63], v[60:61], off
	s_nop 0
	global_load_dwordx4 v[64:67], v[64:65], off
	s_nop 0
	global_load_dwordx4 v[68:71], v[68:69], off
	v_lshlrev_b64 v[76:77], 9, v[54:55]
	v_lshlrev_b64 v[54:55], 13, v[54:55]
	v_lshl_add_u64 v[76:77], s[2:3], 0, v[76:77]
	v_lshl_add_u64 v[54:55], s[52:53], 0, v[54:55]
	v_lshl_add_u64 v[76:77], v[76:77], 0, v[52:53]
	global_load_dwordx4 v[140:143], v[74:75], off
	global_load_dwordx4 v[136:139], v[76:77], off
	v_lshl_add_u64 v[52:53], v[54:55], 0, v[52:53]
	global_load_dwordx4 v[132:135], v[72:73], off
	global_load_dwordx4 v[128:131], v[52:53], off
	v_mov_b32_e32 v82, v81
	s_nop 1
	v_permlane32_swap_b32_e32 v81, v82
	v_max_f32_e32 v52, v82, v82
	v_max_f32_e32 v53, v81, v81
	v_max_f32_e32 v52, v53, v52
	v_add_f32_e32 v53, 0x7149f2ca, v52
	v_max_f32_e32 v52, 0xf149f2ca, v52
	v_cmp_ge_f32_e32 vcc, s9, v53
	v_sub_f32_e32 v53, 0xf149f2ca, v52
	v_mul_f32_e32 v53, 0x3e0293ee, v53
	v_exp_f32_e32 v53, v53
	s_cmp_eq_u64 vcc, exec
	s_cselect_b64 vcc, -1, 0
	v_mov_b32_e32 v54, 0xf149f2ca
	v_cndmask_b32_e32 v160, v52, v54, vcc
	v_mul_f32_e32 v52, 0xbe0293ee, v160
	v_cndmask_b32_e64 v205, v53, 1.0, vcc
	v_mov_b32_e32 v53, v52
	v_fmac_f32_e32 v53, 0x3e0293ee, v47
	v_pk_fma_f32 v[150:151], v[18:19], s[8:9], v[52:53] op_sel_hi:[1,0,0]
	v_pk_fma_f32 v[152:153], v[16:17], s[8:9], v[52:53] op_sel_hi:[1,0,0]
	v_lshl_add_u64 v[16:17], s[4:5], 0, v[50:51]
	v_and_b32_e32 v18, 0xf0, v78
	v_fmamk_f32 v32, v32, 0x3e0293ee, v52
	v_fmamk_f32 v33, v33, 0x3e0293ee, v52
	v_fmamk_f32 v34, v34, 0x3e0293ee, v52
	v_fmamk_f32 v35, v35, 0x3e0293ee, v52
	v_fmamk_f32 v36, v36, 0x3e0293ee, v52
	v_fmamk_f32 v37, v37, 0x3e0293ee, v52
	v_fmamk_f32 v38, v38, 0x3e0293ee, v52
	v_fmamk_f32 v39, v39, 0x3e0293ee, v52
	v_fmamk_f32 v40, v40, 0x3e0293ee, v52
	v_fmamk_f32 v41, v41, 0x3e0293ee, v52
	v_fmamk_f32 v42, v42, 0x3e0293ee, v52
	v_fmamk_f32 v43, v43, 0x3e0293ee, v52
	v_fmamk_f32 v44, v44, 0x3e0293ee, v52
	v_fmamk_f32 v45, v45, 0x3e0293ee, v52
	v_fmamk_f32 v46, v46, 0x3e0293ee, v52
	v_or_b32_e32 v16, v16, v18
	v_exp_f32_e32 v170, v32
	v_exp_f32_e32 v171, v33
	v_exp_f32_e32 v172, v34
	v_exp_f32_e32 v173, v35
	v_exp_f32_e32 v174, v36
	v_exp_f32_e32 v184, v37
	v_exp_f32_e32 v175, v38
	v_exp_f32_e32 v185, v39
	v_exp_f32_e32 v162, v40
	v_exp_f32_e32 v163, v41
	v_exp_f32_e32 v164, v42
	v_exp_f32_e32 v166, v43
	v_exp_f32_e32 v165, v44
	v_exp_f32_e32 v167, v45
	v_exp_f32_e32 v168, v46
	v_exp_f32_e32 v169, v53
	v_lshl_add_u64 v[180:181], s[24:25], 0, v[16:17]
	v_lshl_add_u64 v[16:17], s[28:29], 0, v[48:49]
	s_waitcnt vmcnt(4)
	v_or_b32_e32 v16, v16, v18
	v_mov_b64_e32 v[12:13], s[48:49]
	v_pk_fma_f32 v[154:155], v[30:31], s[8:9], v[52:53] op_sel_hi:[1,0,0]
	v_pk_fma_f32 v[156:157], v[28:29], s[8:9], v[52:53] op_sel_hi:[1,0,0]
	v_pk_fma_f32 v[158:159], v[26:27], s[8:9], v[52:53] op_sel_hi:[1,0,0]
	v_pk_fma_f32 v[144:145], v[24:25], s[8:9], v[52:53] op_sel_hi:[1,0,0]
	v_pk_fma_f32 v[146:147], v[22:23], s[8:9], v[52:53] op_sel_hi:[1,0,0]
	v_pk_fma_f32 v[148:149], v[20:21], s[8:9], v[52:53] op_sel_hi:[1,0,0]
	s_waitcnt vmcnt(7)
	ds_write_b128 v193, v[56:59] offset:16384
	s_waitcnt vmcnt(6)
	ds_write_b128 v194, v[60:63] offset:16384
	s_waitcnt vmcnt(5)
	ds_write_b128 v195, v[64:67] offset:49152
	s_waitcnt vmcnt(4)
	ds_write_b128 v196, v[68:71] offset:49152
	s_addk_i32 s58, 0x4000
	v_lshl_add_u64 v[182:183], s[24:25], 0, v[16:17]
	v_mov_b64_e32 v[62:63], v[14:15]
	v_mov_b64_e32 v[30:31], v[14:15]
	v_mov_b64_e32 v[46:47], v[14:15]
	v_cmp_gt_u32_e64 s[2:3], 32, v79
	v_add_u32_e32 v191, s58, v80
	v_mov_b64_e32 v[60:61], v[12:13]
	v_mov_b64_e32 v[58:59], v[10:11]
	v_mov_b64_e32 v[56:57], v[8:9]
	v_mov_b64_e32 v[54:55], v[6:7]
	v_mov_b64_e32 v[52:53], v[4:5]
	v_mov_b64_e32 v[50:51], v[2:3]
	v_mov_b64_e32 v[48:49], v[0:1]
	v_mov_b64_e32 v[28:29], v[12:13]
	v_mov_b64_e32 v[26:27], v[10:11]
	v_mov_b64_e32 v[24:25], v[8:9]
	v_mov_b64_e32 v[22:23], v[6:7]
	v_mov_b64_e32 v[20:21], v[4:5]
	v_mov_b64_e32 v[18:19], v[2:3]
	v_mov_b64_e32 v[16:17], v[0:1]
	v_mov_b64_e32 v[44:45], v[12:13]
	v_mov_b64_e32 v[42:43], v[10:11]
	v_mov_b64_e32 v[40:41], v[8:9]
	v_mov_b64_e32 v[38:39], v[6:7]
	v_mov_b64_e32 v[36:37], v[4:5]
	v_mov_b64_e32 v[34:35], v[2:3]
	v_mov_b64_e32 v[32:33], v[0:1]
	s_waitcnt lgkmcnt(0)
	s_barrier

.LBB0_2189:
	s_load_dwordx2 s[30:31], s[2:3], 0x78
	s_ashr_i32 s2, s57, 4
	s_mul_hi_i32 s3, s2, 0x2aaaaaab
	s_lshr_b32 s4, s3, 31
	s_add_i32 s3, s3, s4
	s_mul_i32 s3, s3, 6
	s_sub_i32 s2, s2, s3
	s_mul_hi_i32 s3, s57, 0x2aaaaaab
	s_lshr_b32 s4, s3, 31
	s_ashr_i32 s3, s3, 4
	s_add_i32 s28, s3, s4
	s_mul_i32 s3, s2, 0x56
	s_lshr_b32 s4, s3, 8
	s_bfe_u32 s3, s3, 0x1000f
	s_add_i32 s4, s4, s3
	s_ashr_i32 s29, s28, 31
	s_lshl_b32 s3, s57, 8
	s_lshl_b64 s[34:35], s[28:29], 12
	s_and_b32 s3, s3, 0xf00
	s_or_b32 s34, s34, s3
	s_sext_i32_i8 s37, s4
	s_mul_i32 s3, s35, 0x600
	s_mul_hi_u32 s4, s34, 0x600
	s_add_i32 s4, s4, s3
	s_mul_i32 s3, s34, 0x600
	s_add_u32 s5, s26, s3
	s_addc_u32 s4, s27, s4
	s_lshl_b32 s24, s2, 7
	s_ashr_i32 s25, s24, 31
	s_lshl_b64 s[2:3], s[24:25], 1
	s_add_u32 s2, s5, s2
	s_addc_u32 s3, s4, s3
	s_add_u32 s38, s2, 0x48560200
	s_addc_u32 s39, s3, 0
	s_lshl_b64 s[4:5], s[28:29], 21
	s_add_u32 s40, s26, s4
	s_addc_u32 s41, s27, s5
	s_lshl_b32 s2, s37, 7
	s_ashr_i32 s3, s2, 31
	s_lshl_b64 s[52:53], s[2:3], 1
	s_add_u32 s2, s40, s52
	s_addc_u32 s3, s41, s53
	s_add_u32 s2, s2, 0x49d60200
	s_addc_u32 s3, s3, 0
	s_lshl_b64 s[28:29], s[28:29], 25
	s_add_u32 s37, s26, s28
	s_addc_u32 s40, s27, s29
	s_add_u32 s37, s37, s52
	s_waitcnt lgkmcnt(0)
	s_addc_u32 s40, s40, s53
	s_add_u32 s54, s37, 0x40560a00
	v_ashrrev_i32_e32 v54, 4, v0
	v_lshlrev_b32_e32 v1, 3, v0
	v_ashrrev_i32_e32 v55, 31, v54
	s_addc_u32 s55, s40, 0
	v_and_b32_e32 v2, 0x78, v1
	v_lshlrev_b64 v[48:49], 13, v[54:55]
	v_lshlrev_b32_e32 v52, 1, v2
	v_add_u32_e32 v18, 32, v54
	v_lshl_add_u64 v[2:3], s[54:55], 0, v[48:49]
	v_mov_b32_e32 v53, v177
	v_lshl_add_u64 v[2:3], v[2:3], 0, v[52:53]
	v_ashrrev_i32_e32 v19, 31, v18
	global_load_dwordx4 v[2:5], v[2:3], off
	v_lshlrev_b64 v[6:7], 13, v[18:19]
	v_lshlrev_b64 v[50:51], 9, v[54:55]
	v_lshl_add_u64 v[6:7], s[54:55], 0, v[6:7]
	v_lshl_add_u64 v[10:11], s[2:3], 0, v[50:51]
	v_lshl_add_u64 v[6:7], v[6:7], 0, v[52:53]
	v_lshl_add_u64 v[10:11], v[10:11], 0, v[52:53]
	global_load_dwordx4 v[6:9], v[6:7], off
	v_lshlrev_b64 v[14:15], 9, v[18:19]
	global_load_dwordx4 v[10:13], v[10:11], off
	v_lshl_add_u64 v[14:15], s[2:3], 0, v[14:15]
	v_lshl_add_u64 v[14:15], v[14:15], 0, v[52:53]
	v_readfirstlane_b32 s37, v0
	global_load_dwordx4 v[14:17], v[14:15], off
	s_ashr_i32 s40, s37, 1
	v_mov_b32_e32 v19, s40
	v_bfe_u32 v189, v0, 5, 1
	v_bfi_b32 v19, s1, v19, v0
	v_mov_b64_e32 v[20:21], s[38:39]
	v_mad_i64_i32 v[20:21], s[38:39], v19, s0, v[20:21]
	v_lshlrev_b32_e32 v176, 4, v189
	v_lshl_add_u64 v[20:21], v[20:21], 0, v[176:177]
	global_load_dwordx4 v[124:127], v[20:21], off
	global_load_dwordx4 v[120:123], v[20:21], off offset:32
	global_load_dwordx4 v[116:119], v[20:21], off offset:64
	global_load_dwordx4 v[112:115], v[20:21], off offset:96
	global_load_dwordx4 v[108:111], v[20:21], off offset:128
	global_load_dwordx4 v[104:107], v[20:21], off offset:160
	global_load_dwordx4 v[100:103], v[20:21], off offset:192
	global_load_dwordx4 v[96:99], v[20:21], off offset:224
	v_and_b32_e32 v19, 0xfffff0, v54
	v_lshlrev_b32_e32 v20, 1, v54
	v_and_or_b32 v19, v20, 8, v19
	v_and_b32_e32 v22, 0xfffff0, v18
	v_lshlrev_b32_e32 v23, 1, v18
	v_lshrrev_b32_e32 v20, 1, v54
	v_lshrrev_b32_e32 v19, 1, v19
	v_bfe_u32 v1, v1, 5, 2
	v_and_b32_e32 v21, 3, v54
	v_and_or_b32 v22, v23, 8, v22
	v_or_b32_e32 v19, v19, v1
	v_and_or_b32 v20, v20, 4, v21
	v_lshrrev_b32_e32 v22, 1, v22
	v_lshlrev_b32_e32 v19, 9, v19
	v_lshlrev_b32_e32 v20, 6, v20
	v_and_b32_e32 v21, 48, v52
	v_or_b32_e32 v1, v22, v1
	v_or3_b32 v19, v19, v20, v21
	v_lshlrev_b32_e32 v1, 9, v1
	v_or3_b32 v1, v1, v20, v21
	v_add_u32_e32 v193, 0, v19
	s_waitcnt vmcnt(0)
	v_add_u32_e32 v194, 0, v1
	v_lshlrev_b32_e32 v1, 8, v54
	v_and_b32_e32 v178, 31, v0
	v_lshlrev_b32_e32 v78, 4, v0
	v_and_b32_e32 v79, 63, v0
	v_add_u32_e32 v64, 64, v54
	v_add_u32_e32 v66, 0x60, v54
	v_ashrrev_i32_e32 v65, 31, v64
	v_ashrrev_i32_e32 v67, 31, v66
	v_add_u32_e32 v72, 0xa0, v54
	v_ashrrev_i32_e32 v73, 31, v72
	v_add_u32_e32 v54, 0x80, v54
	v_lshlrev_b64 v[74:75], 9, v[72:73]
	v_lshlrev_b64 v[72:73], 13, v[72:73]
	v_lshl_add_u64 v[74:75], s[2:3], 0, v[74:75]
	v_lshl_add_u64 v[72:73], s[54:55], 0, v[72:73]
	v_lshl_add_u64 v[74:75], v[74:75], 0, v[52:53]
	v_lshl_add_u64 v[72:73], v[72:73], 0, v[52:53]
	s_and_b32 s37, s37, 0x3fffffc0
	s_lshl_b32 s37, s37, 2
	s_add_i32 s59, s37, 0
	s_add_i32 s59, s59, 0x10000
	s_and_b32 s58, s40, 0xffffffe0
	s_cmp_lg_u32 0, -1
	s_cselect_b32 s61, 0, 0
	s_mov_b32 s37, s36
	s_mov_b32 s38, s36
	s_mov_b32 s39, s36
	s_mov_b32 s40, s36
	s_mov_b32 s41, s36
	s_mov_b32 s42, s36
	s_mov_b32 s43, s36
	s_mov_b32 s44, s36
	s_waitcnt vmcnt(11)
	ds_write_b128 v193, v[2:5]
	v_and_b32_e32 v2, 0xf0, v0
	v_bitop3_b32 v1, v52, v1, v2 bitop3:0xde
	v_add_u32_e32 v195, 0, v1
	v_lshlrev_b32_e32 v1, 8, v18
	v_bitop3_b32 v1, v52, v1, v2 bitop3:0xde
	v_add_u32_e32 v196, 0, v1
	s_waitcnt vmcnt(10)
	ds_write_b128 v194, v[6:9]
	s_mov_b32 s45, s36
	s_waitcnt vmcnt(9)
	ds_write_b128 v195, v[10:13] offset:32768
	v_lshlrev_b32_e32 v10, 8, v178
	v_and_b32_e32 v11, 0xf0, v78
	v_bitop3_b32 v1, v176, v10, v11 bitop3:0xde
	v_add_u32_e32 v197, 0, v1
	s_waitcnt vmcnt(8)
	ds_write_b128 v196, v[14:17] offset:32768
	s_waitcnt lgkmcnt(0)
	s_barrier
	ds_read_b128 v[2:5], v197 offset:32768
	ds_read_b128 v[6:9], v197 offset:40960
	s_waitcnt vmcnt(7) lgkmcnt(1)
	v_mfma_f32_32x32x16_bf16 v[32:47], v[2:5], v[124:127], 0
	v_or_b32_e32 v1, 32, v176
	v_bitop3_b32 v1, v1, v10, v11 bitop3:0xde
	v_add_u32_e32 v198, 0, v1
	v_or_b32_e32 v1, 64, v176
	v_bitop3_b32 v1, v1, v10, v11 bitop3:0xde
	v_add_u32_e32 v199, 0, v1
	v_or_b32_e32 v1, 0x60, v176
	s_waitcnt lgkmcnt(0)
	v_mfma_f32_32x32x16_bf16 v[16:31], v[6:9], v[124:127], 0
	ds_read_b128 v[2:5], v198 offset:32768
	ds_read_b128 v[6:9], v198 offset:40960
	v_bitop3_b32 v1, v1, v10, v11 bitop3:0xde
	v_add_u32_e32 v200, 0, v1
	v_or_b32_e32 v1, 0x80, v176
	v_bitop3_b32 v1, v1, v10, v11 bitop3:0xde
	v_add_u32_e32 v201, 0, v1
	v_or_b32_e32 v1, 0xa0, v176
	s_waitcnt vmcnt(6) lgkmcnt(1)
	v_mfma_f32_32x32x16_bf16 v[32:47], v[2:5], v[120:123], v[32:47]
	v_bitop3_b32 v1, v1, v10, v11 bitop3:0xde
	v_add_u32_e32 v202, 0, v1
	v_lshlrev_b32_e32 v12, 3, v79
	v_and_b32_e32 v1, 0xc0, v78
	s_mov_b32 s46, s36
	s_mov_b32 s47, s36
	s_mov_b32 s48, s36
	s_waitcnt lgkmcnt(0)
	v_mfma_f32_32x32x16_bf16 v[16:31], v[6:9], v[120:123], v[16:31]
	ds_read_b128 v[2:5], v199 offset:32768
	ds_read_b128 v[6:9], v199 offset:40960
	s_mov_b32 s49, s36
	s_mov_b32 s50, s36
	s_mov_b32 s51, s36
	s_mov_b32 s60, 1
	v_lshl_add_u32 v179, v178, 2, s59
	v_mov_b32_e32 v190, 0
	s_waitcnt vmcnt(5) lgkmcnt(1)
	v_mfma_f32_32x32x16_bf16 v[32:47], v[2:5], v[116:119], v[32:47]
	s_waitcnt lgkmcnt(0)
	v_mfma_f32_32x32x16_bf16 v[16:31], v[6:9], v[116:119], v[16:31]
	ds_read_b128 v[2:5], v200 offset:32768
	ds_read_b128 v[6:9], v200 offset:40960
	s_waitcnt vmcnt(4) lgkmcnt(1)
	v_mfma_f32_32x32x16_bf16 v[32:47], v[2:5], v[112:115], v[32:47]
	s_waitcnt lgkmcnt(0)
	v_mfma_f32_32x32x16_bf16 v[16:31], v[6:9], v[112:115], v[16:31]
	ds_read_b128 v[2:5], v201 offset:32768
	ds_read_b128 v[6:9], v201 offset:40960
	s_waitcnt vmcnt(3) lgkmcnt(1)
	v_mfma_f32_32x32x16_bf16 v[32:47], v[2:5], v[108:111], v[32:47]
	ds_read_b128 v[2:5], v202 offset:32768
	s_waitcnt lgkmcnt(1)
	v_mfma_f32_32x32x16_bf16 v[16:31], v[6:9], v[108:111], v[16:31]
	ds_read_b128 v[6:9], v202 offset:40960
	s_waitcnt vmcnt(2) lgkmcnt(1)
	v_mfma_f32_32x32x16_bf16 v[32:47], v[2:5], v[104:107], v[32:47]
	v_lshlrev_b32_e32 v5, 1, v0
	v_or_b32_e32 v0, 0xc0, v176
	v_bitop3_b32 v0, v0, v10, v11 bitop3:0xde
	v_add_u32_e32 v203, 0, v0
	v_and_or_b32 v4, v12, 24, v1
	ds_read_b128 v[0:3], v203 offset:32768
	v_and_b32_e32 v5, 32, v5
	s_waitcnt lgkmcnt(1)
	v_mfma_f32_32x32x16_bf16 v[16:31], v[6:9], v[104:107], v[16:31]
	v_lshlrev_b32_e32 v6, 3, v12
	v_and_b32_e32 v6, 0x800, v6
	v_or3_b32 v80, v4, v5, v6
	ds_read_b128 v[4:7], v203 offset:40960
	v_add_u32_e32 v192, s61, v80
	s_waitcnt vmcnt(1) lgkmcnt(1)
	v_mfma_f32_32x32x16_bf16 v[32:47], v[0:3], v[100:103], v[32:47]
	v_or_b32_e32 v0, 0xe0, v176
	v_bitop3_b32 v0, v0, v10, v11 bitop3:0xde
	v_add_u32_e32 v204, 0, v0
	ds_read_b128 v[0:3], v204 offset:32768
	ds_read_b128 v[56:59], v204 offset:40960
	s_waitcnt lgkmcnt(2)
	v_mfma_f32_32x32x16_bf16 v[16:31], v[4:7], v[100:103], v[16:31]
	s_waitcnt vmcnt(0) lgkmcnt(1)
	v_mfma_f32_32x32x16_bf16 v[32:47], v[0:3], v[96:99], v[32:47]
	v_mov_b64_e32 v[0:1], s[36:37]
	v_mov_b64_e32 v[14:15], s[50:51]
	v_mov_b64_e32 v[2:3], s[38:39]
	v_mov_b64_e32 v[4:5], s[40:41]
	v_mov_b64_e32 v[6:7], s[42:43]
	v_mov_b64_e32 v[8:9], s[44:45]
	v_mov_b64_e32 v[10:11], s[46:47]
	s_waitcnt lgkmcnt(0)
	v_mfma_f32_32x32x16_bf16 v[16:31], v[56:59], v[96:99], v[16:31]
	s_nop 2
	v_max_f32_e32 v55, v33, v33
	v_max_f32_e32 v56, v32, v32
	v_max_f32_e32 v55, v56, v55
	v_max3_f32 v55, v55, v34, v35
	v_max3_f32 v55, v55, v36, v37
	v_max3_f32 v55, v55, v38, v39
	v_max3_f32 v55, v55, v40, v41
	v_max3_f32 v55, v55, v42, v43
	v_max3_f32 v55, v55, v44, v45
	v_max3_f32 v55, v55, v46, v47
	v_max3_f32 v55, v55, v16, v17
	v_max3_f32 v55, v55, v18, v19
	v_max3_f32 v55, v55, v20, v21
	v_max3_f32 v55, v55, v22, v23
	v_max3_f32 v55, v55, v24, v25
	v_max3_f32 v55, v55, v26, v27
	v_lshlrev_b64 v[56:57], 13, v[64:65]
	v_lshlrev_b64 v[58:59], 13, v[66:67]
	v_lshlrev_b64 v[64:65], 9, v[64:65]
	v_lshlrev_b64 v[66:67], 9, v[66:67]
	v_max3_f32 v55, v55, v28, v29
	v_lshl_add_u64 v[56:57], s[54:55], 0, v[56:57]
	v_lshl_add_u64 v[58:59], s[54:55], 0, v[58:59]
	v_lshl_add_u64 v[64:65], s[2:3], 0, v[64:65]
	v_lshl_add_u64 v[66:67], s[2:3], 0, v[66:67]
	v_max3_f32 v81, v55, v30, v31
	v_lshl_add_u64 v[56:57], v[56:57], 0, v[52:53]
	v_lshl_add_u64 v[60:61], v[58:59], 0, v[52:53]
	v_lshl_add_u64 v[64:65], v[64:65], 0, v[52:53]
	v_lshl_add_u64 v[68:69], v[66:67], 0, v[52:53]
	v_ashrrev_i32_e32 v55, 31, v54
	global_load_dwordx4 v[56:59], v[56:57], off
	s_nop 0
	global_load_dwordx4 v[60:63], v[60:61], off
	s_nop 0
	global_load_dwordx4 v[64:67], v[64:65], off
	s_nop 0
	global_load_dwordx4 v[68:71], v[68:69], off
	v_lshlrev_b64 v[76:77], 9, v[54:55]
	v_lshlrev_b64 v[54:55], 13, v[54:55]
	v_lshl_add_u64 v[76:77], s[2:3], 0, v[76:77]
	v_lshl_add_u64 v[54:55], s[54:55], 0, v[54:55]
	v_lshl_add_u64 v[76:77], v[76:77], 0, v[52:53]
	global_load_dwordx4 v[140:143], v[74:75], off
	global_load_dwordx4 v[136:139], v[76:77], off
	v_lshl_add_u64 v[52:53], v[54:55], 0, v[52:53]
	global_load_dwordx4 v[132:135], v[72:73], off
	global_load_dwordx4 v[128:131], v[52:53], off
	v_mov_b32_e32 v82, v81
	s_nop 1
	v_permlane32_swap_b32_e32 v81, v82
	v_max_f32_e32 v52, v82, v82
	v_max_f32_e32 v53, v81, v81
	v_max_f32_e32 v52, v53, v52
	v_add_f32_e32 v53, 0x7149f2ca, v52
	v_max_f32_e32 v52, 0xf149f2ca, v52
	v_cmp_ge_f32_e32 vcc, s9, v53
	v_sub_f32_e32 v53, 0xf149f2ca, v52
	v_mul_f32_e32 v53, 0x3e0293ee, v53
	v_exp_f32_e32 v53, v53
	s_cmp_eq_u64 vcc, exec
	s_cselect_b64 vcc, -1, 0
	v_cndmask_b32_e32 v160, v52, v188, vcc
	v_mul_f32_e32 v52, 0xbe0293ee, v160
	v_cndmask_b32_e64 v205, v53, 1.0, vcc
	v_mov_b32_e32 v53, v52
	v_fmac_f32_e32 v53, 0x3e0293ee, v47
	v_pk_fma_f32 v[150:151], v[18:19], s[8:9], v[52:53] op_sel_hi:[1,0,0]
	v_pk_fma_f32 v[152:153], v[16:17], s[8:9], v[52:53] op_sel_hi:[1,0,0]
	v_lshl_add_u64 v[16:17], s[4:5], 0, v[50:51]
	v_and_b32_e32 v18, 0xf0, v78
	v_fmamk_f32 v32, v32, 0x3e0293ee, v52
	v_fmamk_f32 v33, v33, 0x3e0293ee, v52
	v_fmamk_f32 v34, v34, 0x3e0293ee, v52
	v_fmamk_f32 v35, v35, 0x3e0293ee, v52
	v_fmamk_f32 v36, v36, 0x3e0293ee, v52
	v_fmamk_f32 v37, v37, 0x3e0293ee, v52
	v_fmamk_f32 v38, v38, 0x3e0293ee, v52
	v_fmamk_f32 v39, v39, 0x3e0293ee, v52
	v_fmamk_f32 v40, v40, 0x3e0293ee, v52
	v_fmamk_f32 v41, v41, 0x3e0293ee, v52
	v_fmamk_f32 v42, v42, 0x3e0293ee, v52
	v_fmamk_f32 v43, v43, 0x3e0293ee, v52
	v_fmamk_f32 v44, v44, 0x3e0293ee, v52
	v_fmamk_f32 v45, v45, 0x3e0293ee, v52
	v_fmamk_f32 v46, v46, 0x3e0293ee, v52
	v_or_b32_e32 v16, v16, v18
	v_exp_f32_e32 v170, v32
	v_exp_f32_e32 v171, v33
	v_exp_f32_e32 v172, v34
	v_exp_f32_e32 v173, v35
	v_exp_f32_e32 v174, v36
	v_exp_f32_e32 v184, v37
	v_exp_f32_e32 v175, v38
	v_exp_f32_e32 v185, v39
	v_exp_f32_e32 v162, v40
	v_exp_f32_e32 v163, v41
	v_exp_f32_e32 v164, v42
	v_exp_f32_e32 v166, v43
	v_exp_f32_e32 v165, v44
	v_exp_f32_e32 v167, v45
	v_exp_f32_e32 v168, v46
	v_exp_f32_e32 v169, v53
	v_lshl_add_u64 v[180:181], s[26:27], 0, v[16:17]
	v_lshl_add_u64 v[16:17], s[28:29], 0, v[48:49]
	s_waitcnt vmcnt(4)
	v_or_b32_e32 v16, v16, v18
	v_mov_b64_e32 v[12:13], s[48:49]
	v_pk_fma_f32 v[154:155], v[30:31], s[8:9], v[52:53] op_sel_hi:[1,0,0]
	v_pk_fma_f32 v[156:157], v[28:29], s[8:9], v[52:53] op_sel_hi:[1,0,0]
	v_pk_fma_f32 v[158:159], v[26:27], s[8:9], v[52:53] op_sel_hi:[1,0,0]
	v_pk_fma_f32 v[144:145], v[24:25], s[8:9], v[52:53] op_sel_hi:[1,0,0]
	v_pk_fma_f32 v[146:147], v[22:23], s[8:9], v[52:53] op_sel_hi:[1,0,0]
	v_pk_fma_f32 v[148:149], v[20:21], s[8:9], v[52:53] op_sel_hi:[1,0,0]
	s_waitcnt vmcnt(7)
	ds_write_b128 v193, v[56:59] offset:16384
	s_waitcnt vmcnt(6)
	ds_write_b128 v194, v[60:63] offset:16384
	s_waitcnt vmcnt(5)
	ds_write_b128 v195, v[64:67] offset:49152
	s_waitcnt vmcnt(4)
	ds_write_b128 v196, v[68:71] offset:49152
	s_addk_i32 s61, 0x4000
	v_lshl_add_u64 v[182:183], s[26:27], 0, v[16:17]
	v_mov_b64_e32 v[62:63], v[14:15]
	v_mov_b64_e32 v[30:31], v[14:15]
	v_mov_b64_e32 v[46:47], v[14:15]
	v_cmp_gt_u32_e64 s[2:3], 32, v79
	v_add_u32_e32 v191, s61, v80
	v_mov_b64_e32 v[60:61], v[12:13]
	v_mov_b64_e32 v[58:59], v[10:11]
	v_mov_b64_e32 v[56:57], v[8:9]
	v_mov_b64_e32 v[54:55], v[6:7]
	v_mov_b64_e32 v[52:53], v[4:5]
	v_mov_b64_e32 v[50:51], v[2:3]
	v_mov_b64_e32 v[48:49], v[0:1]
	v_mov_b64_e32 v[28:29], v[12:13]
	v_mov_b64_e32 v[26:27], v[10:11]
	v_mov_b64_e32 v[24:25], v[8:9]
	v_mov_b64_e32 v[22:23], v[6:7]
	v_mov_b64_e32 v[20:21], v[4:5]
	v_mov_b64_e32 v[18:19], v[2:3]
	v_mov_b64_e32 v[16:17], v[0:1]
	v_mov_b64_e32 v[44:45], v[12:13]
	v_mov_b64_e32 v[42:43], v[10:11]
	v_mov_b64_e32 v[40:41], v[8:9]
	v_mov_b64_e32 v[38:39], v[6:7]
	v_mov_b64_e32 v[36:37], v[4:5]
	v_mov_b64_e32 v[34:35], v[2:3]
	v_mov_b64_e32 v[32:33], v[0:1]
	s_waitcnt lgkmcnt(0)
	s_barrier
